# GLA: preparation waves run at s_setprio 1 (they are the pole of both barrier intervals)
# speedup vs baseline: 1.0062x; 1.0059x over previous
; __device__ __forceinline__ void gla_fast_unit(int unit, const bf16_t* P, const float* w_up, const float* b_up, float* Of, float* Ob, LAS unsigned char* lds0) {
;     ...
;     __syncthreads();
;     if (wv < 4) {
;     ...
;         const int pw = wv - 4, ptid = tid - 256;
;         bf16x8 wfr[4]; float bu[4];
; #pragma unroll
;         for (int it = 0; it < 4; ++it) { unsigned w[4] = {0u, 0u, 0u, 0u};
;             if (q < 2) {
; #pragma unroll
;                 for (int j = 0; j < 4; ++j) w[j] = pk2(w_up[(size_t)(dir * 16 + 8 * q + 2 * j) * 512 + h * 64 + 16 * it + l15], w_up[(size_t)(dir * 16 + 8 * q + 2 * j + 1) * 512 + h * 64 + 16 * it + l15]); }
;             wfr[it] = __builtin_bit_cast(bf16x8, (u32x4){w[0], w[1], w[2], w[3]}); bu[it] = b_up[dir * 512 + h * 64 + 16 * it + l15]; }
.LBB0_1129:
	v_readlane_b32 s2, v254, 0
	s_cmp_lt_i32 s2, 14
	s_cselect_b64 s[22:23], -1, 0
	s_and_b64 s[0:1], s[22:23], s[0:1]
	s_andn2_b64 vcc, exec, s[0:1]
	v_readlane_b32 s3, v254, 1
	s_cbranch_vccnz .LBB0_1316
	v_lshlrev_b32_e32 v2, 4, v0
	v_readlane_b32 s0, v255, 10
	v_bfe_u32 v86, v0, 4, 2
	v_and_b32_e32 v177, 0xf0, v2
	v_or_b32_e32 v2, 0x200, v0
	v_readlane_b32 s1, v255, 11
	v_lshrrev_b32_e32 v168, 4, v0
	v_lshlrev_b32_e32 v169, 2, v86
	v_lshrrev_b32_e32 v170, 4, v2
	v_bfe_u32 v182, v0, 2, 2
	v_lshlrev_b32_e32 v181, 3, v0
	s_cmp_gt_i32 s0, 63
	v_and_b32_e32 v1, 15, v0
	v_lshlrev_b32_e32 v176, 4, v86
	s_mov_b32 s25, 0
	v_cmp_eq_u32_e64 s[0:1], 0, v86
	v_add_u32_e32 v174, 0, v177
	s_movk_i32 s44, 0x120
	v_mul_u32_u24_e32 v171, 0x120, v168
	v_mul_u32_u24_e32 v172, 0x120, v170
	v_lshlrev_b32_e32 v175, 3, v86
	v_and_b32_e32 v178, 24, v181
	v_or_b32_e32 v173, v169, v182
	v_or_b32_e32 v179, 3, v169
	v_or_b32_e32 v180, 2, v169
	v_mov_b32_e32 v87, 0
	s_cbranch_scc1 .LBB0_1206
	v_readlane_b32 s2, v255, 10
	s_and_b32 s8, s2, 1
	s_bfe_u32 s10, s2, 0x30001
	s_ashr_i32 s9, s2, 4
	s_cmp_eq_u32 s8, 0
	v_readfirstlane_b32 s30, v0
	v_readlane_b32 s3, v255, 11
	s_cselect_b64 s[4:5], -1, 0
	s_lshl_b32 s31, s10, 7
	s_lshl_b32 s24, s9, 12
	s_lshr_b32 s34, s30, 6
	s_cmpk_gt_u32 s30, 0xff
	s_mov_b64 s[2:3], -1
	s_waitcnt vmcnt(0) lgkmcnt(0)
	s_barrier
	s_cbranch_scc0 .LBB0_1199
	s_setprio 1
	s_lshl_b32 s2, s8, 13
	s_lshl_b32 s11, s10, 6
	v_lshl_add_u32 v2, v86, 12, s2
	v_or3_b32 v2, v2, s11, v1
	v_readlane_b32 s48, v254, 29
	v_lshlrev_b32_e32 v4, 2, v2
	v_mov_b32_e32 v5, 0
	v_readlane_b32 s54, v254, 35
	v_readlane_b32 s55, v254, 36
	v_cmp_gt_u32_e64 s[6:7], 2, v86
	v_mov_b32_e32 v9, 0
	v_lshl_add_u64 v[12:13], s[54:55], 0, v[4:5]
	v_mov_b32_e32 v8, 0
	v_mov_b32_e32 v7, 0
	v_mov_b32_e32 v6, 0
	v_readlane_b32 s49, v254, 30
	v_readlane_b32 s50, v254, 31
	v_readlane_b32 s51, v254, 32
	v_readlane_b32 s52, v254, 33
	v_readlane_b32 s53, v254, 34
	v_readlane_b32 s56, v254, 37
	v_readlane_b32 s57, v254, 38
	v_readlane_b32 s58, v254, 39
	v_readlane_b32 s59, v254, 40
	v_readlane_b32 s60, v254, 41
	v_readlane_b32 s61, v254, 42
	v_readlane_b32 s62, v254, 43
	v_readlane_b32 s63, v254, 44
	s_and_saveexec_b64 s[2:3], s[6:7]
	s_cbranch_execz .LBB0_1134
	v_add_co_u32_e32 v2, vcc, 0x1000, v12
	s_nop 1
	v_addc_co_u32_e32 v3, vcc, 0, v13, vcc
	v_add_co_u32_e32 v6, vcc, 0x2000, v12
	s_nop 1
	v_addc_co_u32_e32 v7, vcc, 0, v13, vcc
	v_add_co_u32_e32 v8, vcc, 0x3000, v12
	s_nop 1
	v_addc_co_u32_e32 v9, vcc, 0, v13, vcc
	global_load_dword v4, v[12:13], off
	global_load_dword v10, v[12:13], off offset:2048
	global_load_dword v11, v[2:3], off
	s_nop 0
	global_load_dword v2, v[2:3], off offset:2048
	s_nop 0
	global_load_dword v3, v[6:7], off
	global_load_dword v14, v[6:7], off offset:2048
	global_load_dword v15, v[8:9], off
	s_nop 0
	global_load_dword v9, v[8:9], off offset:2048
	s_waitcnt vmcnt(6)
	v_cvt_pk_bf16_f32 v6, v4, v10
	s_waitcnt vmcnt(4)
	v_cvt_pk_bf16_f32 v7, v11, v2
	s_waitcnt vmcnt(2)
	v_cvt_pk_bf16_f32 v8, v3, v14
	s_waitcnt vmcnt(0)
	v_cvt_pk_bf16_f32 v9, v15, v9

; __device__ __forceinline__ void gla_fast_unit(int unit, const bf16_t* P, const float* w_up, const float* b_up, float* Of, float* Ob, LAS unsigned char* lds0) {
;     ...
;         for (int cidx = -1; cidx < NCH + 1; cidx += 2) {
;             GLA_PREP(cidx, graw0, qr0, kr0, vraw0, graw0, qr0, kr0, vraw0);
;             GLA_PREP(cidx + 1, graw0, qr0, kr0, vraw0, graw0, qr0, kr0, vraw0);
;         }
;     ...
;     }
.LBB0_1198:
	s_setprio 0
	s_mov_b64 s[2:3], 0
